# s12 + BR branch epilogue: merged-tile stores write-through (sc1)
# baseline (speedup 1.0000x reference)
;     __device__ __forceinline__ void operator()(const f32x4 (&acc)[2][2][4][2], const Unit& u, int wr, int wc, int fr, int fq) const {
;         const int row0 = u.pm * BM + wr * 64 + fr, col0 = u.pn * BM + wc * 32 + 8 * fq, n = u.z & 3;
;         h16* Gn = Gs + col0;
;         if ((u.z >> 2) == 0) {
; #pragma unroll
;             for (int ai = 0; ai < 2; ++ai)
; #pragma unroll
;                 for (int m = 0; m < 4; ++m) { h16* rowp = Gn + (size_t)(row0 + ai * HALF + m * 16) * ldg;
; #pragma unroll
;                     for (int bj = 0; bj < 2; ++bj) { f32x4 v0 = acc[ai][bj][m][0], v1 = acc[ai][bj][m][1];
; #pragma unroll
;                         for (int e = 0; e < 4; ++e) { v0[e] = __builtin_amdgcn_rcpf(1.f + __expf(-v0[e])); v1[e] = __builtin_amdgcn_rcpf(1.f + __expf(-v1[e])); }
;                         u32x4 w; w.x = cvt_pk_f16(v0[0], v0[1]); w.y = cvt_pk_f16(v0[2], v0[3]); w.z = cvt_pk_f16(v1[0], v1[1]); w.w = cvt_pk_f16(v1[2], v1[3]);
;                         *(u32x4*)(rowp + bj * HALF) = w; } }
;         } else {
; #pragma unroll
;             for (int ai = 0; ai < 2; ++ai)
; #pragma unroll
;                 for (int mp = 0; mp < 2; ++mp) {
;                     h16x8 gv[2][2], pv[2][2];
; #pragma unroll
;                     for (int mm = 0; mm < 2; ++mm)
; #pragma unroll
;                         for (int bj = 0; bj < 2; ++bj) { const size_t row = (size_t)(row0 + ai * HALF + (2 * mp + mm) * 16);
;                             gv[mm][bj] = *(const h16x8*)(Gn + row * ldg + bj * HALF);
;                             if (n > 0) pv[mm][bj] = *(const h16x8*)(Mg + row * 1024 + col0 + bj * HALF); }
; #pragma unroll
;                     for (int mm = 0; mm < 2; ++mm)
; #pragma unroll
;                         for (int bj = 0; bj < 2; ++bj) { const int m = 2 * mp + mm; const size_t row = (size_t)(row0 + ai * HALF + m * 16);
;                             float o[8];
; #pragma unroll
;                             for (int e = 0; e < 8; ++e) { const float a = e < 4 ? acc[ai][bj][m][0][e] : acc[ai][bj][m][1][e - 4]; o[e] = a * (float)gv[mm][bj][e]; }
;                             if (n > 0) {
; #pragma unroll
;                                 for (int e = 0; e < 8; ++e) o[e] += (float)pv[mm][bj][e]; }
;                             u32x4 w; w.x = cvt_pk_f16(o[0], o[1]); w.y = cvt_pk_f16(o[2], o[3]); w.z = cvt_pk_f16(o[4], o[5]); w.w = cvt_pk_f16(o[6], o[7]);
.LBB0_324:
	v_lshl_or_b32 v178, s73, 8, v165
	v_readlane_b32 s0, v253, 62
	v_ashrrev_i32_e32 v179, 31, v178
	v_readlane_b32 s1, v253, 63
	v_lshl_add_u32 v176, s75, 8, v192
	s_cmp_lt_u32 s72, 4
	v_lshl_add_u64 v[174:175], v[178:179], 1, s[0:1]
	s_mov_b64 s[0:1], -1
	s_cbranch_scc1 .LBB0_390
	s_and_b32 s0, s72, 3
	s_cmp_eq_u32 s0, 0
	s_cbranch_scc1 .Lbrepi_n0
	v_readlane_b32 s40, v254, 46
	v_readlane_b32 s41, v254, 47
	v_mov_b32_e32 v241, 0
	s_nop 1
	v_lshl_add_u64 v[180:181], v[178:179], 1, s[40:41]
	v_mov_b32_e32 v238, v176
	v_mad_i64_i32 v[234:235], s[0:1], v238, s91, v[174:175]
	v_lshlrev_b32_e32 v240, 11, v238
	v_lshl_add_u64 v[236:237], v[180:181], 0, v[240:241]
	global_load_dwordx4 v[130:133], v[234:235], off
	global_load_dwordx4 v[138:141], v[236:237], off
	global_load_dwordx4 v[134:137], v[234:235], off offset:256
	global_load_dwordx4 v[142:145], v[236:237], off offset:256
	v_add_u32_e32 v238, 16, v176
	v_mad_i64_i32 v[234:235], s[0:1], v238, s91, v[174:175]
	v_lshlrev_b32_e32 v240, 11, v238
	v_lshl_add_u64 v[236:237], v[180:181], 0, v[240:241]
	global_load_dwordx4 v[146:149], v[234:235], off
	global_load_dwordx4 v[154:157], v[236:237], off
	global_load_dwordx4 v[150:153], v[234:235], off offset:256
	global_load_dwordx4 v[158:161], v[236:237], off offset:256
	s_waitcnt vmcnt(4)
	v_mov_b32_e32 v238, v176
	v_lshlrev_b32_e32 v240, 11, v238
	v_lshl_add_u64 v[236:237], v[180:181], 0, v[240:241]
	v_cvt_f32_f16_e32 v182, v130
	v_cvt_f32_f16_sdwa v183, v130 dst_sel:DWORD dst_unused:UNUSED_PAD src0_sel:WORD_1
	v_cvt_f32_f16_e32 v184, v131
	v_cvt_f32_f16_sdwa v185, v131 dst_sel:DWORD dst_unused:UNUSED_PAD src0_sel:WORD_1
	v_cvt_f32_f16_e32 v186, v132
	v_cvt_f32_f16_sdwa v187, v132 dst_sel:DWORD dst_unused:UNUSED_PAD src0_sel:WORD_1
	v_cvt_f32_f16_e32 v188, v133
	v_cvt_f32_f16_sdwa v189, v133 dst_sel:DWORD dst_unused:UNUSED_PAD src0_sel:WORD_1
	v_cvt_f32_f16_e32 v196, v138
	v_cvt_f32_f16_sdwa v197, v138 dst_sel:DWORD dst_unused:UNUSED_PAD src0_sel:WORD_1
	v_cvt_f32_f16_e32 v198, v139
	v_cvt_f32_f16_sdwa v199, v139 dst_sel:DWORD dst_unused:UNUSED_PAD src0_sel:WORD_1
	v_cvt_f32_f16_e32 v200, v140
	v_cvt_f32_f16_sdwa v201, v140 dst_sel:DWORD dst_unused:UNUSED_PAD src0_sel:WORD_1
	v_cvt_f32_f16_e32 v202, v141
	v_cvt_f32_f16_sdwa v203, v141 dst_sel:DWORD dst_unused:UNUSED_PAD src0_sel:WORD_1
	v_pk_mul_f32 v[182:183], v[126:127], v[182:183]
	v_pk_mul_f32 v[184:185], v[128:129], v[184:185]
	v_pk_mul_f32 v[186:187], v[122:123], v[186:187]
	v_pk_mul_f32 v[188:189], v[124:125], v[188:189]
	v_pk_add_f32 v[182:183], v[182:183], v[196:197]
	v_pk_add_f32 v[184:185], v[184:185], v[198:199]
	v_pk_add_f32 v[186:187], v[186:187], v[200:201]
	v_pk_add_f32 v[188:189], v[188:189], v[202:203]
	v_cvt_pk_f16_f32 v126, v182, v183
	v_cvt_pk_f16_f32 v127, v184, v185
	v_cvt_pk_f16_f32 v128, v186, v187
	v_cvt_pk_f16_f32 v129, v188, v189
	global_store_dwordx4 v[236:237], v[126:129], off sc1
	v_cvt_f32_f16_e32 v182, v134
	v_cvt_f32_f16_sdwa v183, v134 dst_sel:DWORD dst_unused:UNUSED_PAD src0_sel:WORD_1
	v_cvt_f32_f16_e32 v184, v135
	v_cvt_f32_f16_sdwa v185, v135 dst_sel:DWORD dst_unused:UNUSED_PAD src0_sel:WORD_1
	v_cvt_f32_f16_e32 v186, v136
	v_cvt_f32_f16_sdwa v187, v136 dst_sel:DWORD dst_unused:UNUSED_PAD src0_sel:WORD_1
	v_cvt_f32_f16_e32 v188, v137
	v_cvt_f32_f16_sdwa v189, v137 dst_sel:DWORD dst_unused:UNUSED_PAD src0_sel:WORD_1
	v_cvt_f32_f16_e32 v196, v142
	v_cvt_f32_f16_sdwa v197, v142 dst_sel:DWORD dst_unused:UNUSED_PAD src0_sel:WORD_1
	v_cvt_f32_f16_e32 v198, v143
	v_cvt_f32_f16_sdwa v199, v143 dst_sel:DWORD dst_unused:UNUSED_PAD src0_sel:WORD_1
	v_cvt_f32_f16_e32 v200, v144
	v_cvt_f32_f16_sdwa v201, v144 dst_sel:DWORD dst_unused:UNUSED_PAD src0_sel:WORD_1
	v_cvt_f32_f16_e32 v202, v145
	v_cvt_f32_f16_sdwa v203, v145 dst_sel:DWORD dst_unused:UNUSED_PAD src0_sel:WORD_1
	v_pk_mul_f32 v[182:183], v[118:119], v[182:183]
	v_pk_mul_f32 v[184:185], v[120:121], v[184:185]
	v_pk_mul_f32 v[186:187], v[114:115], v[186:187]
	v_pk_mul_f32 v[188:189], v[116:117], v[188:189]
	v_pk_add_f32 v[182:183], v[182:183], v[196:197]
	v_pk_add_f32 v[184:185], v[184:185], v[198:199]
	v_pk_add_f32 v[186:187], v[186:187], v[200:201]
	v_pk_add_f32 v[188:189], v[188:189], v[202:203]
	v_cvt_pk_f16_f32 v118, v182, v183
	v_cvt_pk_f16_f32 v119, v184, v185
	v_cvt_pk_f16_f32 v120, v186, v187
	v_cvt_pk_f16_f32 v121, v188, v189
	global_store_dwordx4 v[236:237], v[118:121], off offset:256 sc1
	v_add_u32_e32 v238, 32, v176
	v_mad_i64_i32 v[234:235], s[0:1], v238, s91, v[174:175]
	v_lshlrev_b32_e32 v240, 11, v238
	v_lshl_add_u64 v[236:237], v[180:181], 0, v[240:241]
	global_load_dwordx4 v[130:133], v[234:235], off
	global_load_dwordx4 v[138:141], v[236:237], off
	global_load_dwordx4 v[134:137], v[234:235], off offset:256
	global_load_dwordx4 v[142:145], v[236:237], off offset:256
	s_nop 1
	v_add_u32_e32 v238, 48, v176
	v_mad_i64_i32 v[234:235], s[0:1], v238, s91, v[174:175]
	v_lshlrev_b32_e32 v240, 11, v238
	v_lshl_add_u64 v[236:237], v[180:181], 0, v[240:241]
	global_load_dwordx4 v[126:129], v[234:235], off
	global_load_dwordx4 v[118:121], v[236:237], off
	global_load_dwordx4 v[122:125], v[234:235], off offset:256
	global_load_dwordx4 v[114:117], v[236:237], off offset:256
	s_waitcnt vmcnt(10)
; __device__ __forceinline__ unsigned cvt_pk_f16(float lo, float hi) { f32x2 v = {lo, hi}; h16x2 b = __builtin_convertvector(v, h16x2); return __builtin_bit_cast(unsigned, b); }
;     __device__ __forceinline__ void operator()(const f32x4 (&acc)[2][2][4][2], const Unit& u, int wr, int wc, int fr, int fq) const {
;     ...
;         } else {
; #pragma unroll
;             for (int ai = 0; ai < 2; ++ai)
; #pragma unroll
;                 for (int mp = 0; mp < 2; ++mp) {
;                     h16x8 gv[2][2], pv[2][2];
; #pragma unroll
;                     for (int mm = 0; mm < 2; ++mm)
; #pragma unroll
;                         for (int bj = 0; bj < 2; ++bj) { const size_t row = (size_t)(row0 + ai * HALF + (2 * mp + mm) * 16);
;                             gv[mm][bj] = *(const h16x8*)(Gn + row * ldg + bj * HALF);
;                             if (n > 0) pv[mm][bj] = *(const h16x8*)(Mg + row * 1024 + col0 + bj * HALF); }
; #pragma unroll
;                     for (int mm = 0; mm < 2; ++mm)
; #pragma unroll
;                         for (int bj = 0; bj < 2; ++bj) { const int m = 2 * mp + mm; const size_t row = (size_t)(row0 + ai * HALF + m * 16);
;                             float o[8];
; #pragma unroll
;                             for (int e = 0; e < 8; ++e) { const float a = e < 4 ? acc[ai][bj][m][0][e] : acc[ai][bj][m][1][e - 4]; o[e] = a * (float)gv[mm][bj][e]; }
;                             if (n > 0) {
; #pragma unroll
;                                 for (int e = 0; e < 8; ++e) o[e] += (float)pv[mm][bj][e]; }
;                             u32x4 w; w.x = cvt_pk_f16(o[0], o[1]); w.y = cvt_pk_f16(o[2], o[3]); w.z = cvt_pk_f16(o[4], o[5]); w.w = cvt_pk_f16(o[6], o[7]);
;                             *(u32x4*)(Mg + row * 1024 + col0 + bj * HALF) = w; }
;                 }
	v_add_u32_e32 v238, 16, v176
	v_lshlrev_b32_e32 v240, 11, v238
	v_lshl_add_u64 v[236:237], v[180:181], 0, v[240:241]
	v_cvt_f32_f16_e32 v182, v146
	v_cvt_f32_f16_sdwa v183, v146 dst_sel:DWORD dst_unused:UNUSED_PAD src0_sel:WORD_1
	v_cvt_f32_f16_e32 v184, v147
	v_cvt_f32_f16_sdwa v185, v147 dst_sel:DWORD dst_unused:UNUSED_PAD src0_sel:WORD_1
	v_cvt_f32_f16_e32 v186, v148
	v_cvt_f32_f16_sdwa v187, v148 dst_sel:DWORD dst_unused:UNUSED_PAD src0_sel:WORD_1
	v_cvt_f32_f16_e32 v188, v149
	v_cvt_f32_f16_sdwa v189, v149 dst_sel:DWORD dst_unused:UNUSED_PAD src0_sel:WORD_1
	v_cvt_f32_f16_e32 v196, v154
	v_cvt_f32_f16_sdwa v197, v154 dst_sel:DWORD dst_unused:UNUSED_PAD src0_sel:WORD_1
	v_cvt_f32_f16_e32 v198, v155
	v_cvt_f32_f16_sdwa v199, v155 dst_sel:DWORD dst_unused:UNUSED_PAD src0_sel:WORD_1
	v_cvt_f32_f16_e32 v200, v156
	v_cvt_f32_f16_sdwa v201, v156 dst_sel:DWORD dst_unused:UNUSED_PAD src0_sel:WORD_1
	v_cvt_f32_f16_e32 v202, v157
	v_cvt_f32_f16_sdwa v203, v157 dst_sel:DWORD dst_unused:UNUSED_PAD src0_sel:WORD_1
	v_pk_mul_f32 v[182:183], v[110:111], v[182:183]
	v_pk_mul_f32 v[184:185], v[112:113], v[184:185]
	v_pk_mul_f32 v[186:187], v[106:107], v[186:187]
	v_pk_mul_f32 v[188:189], v[108:109], v[188:189]
	v_pk_add_f32 v[182:183], v[182:183], v[196:197]
	v_pk_add_f32 v[184:185], v[184:185], v[198:199]
	v_pk_add_f32 v[186:187], v[186:187], v[200:201]
	v_pk_add_f32 v[188:189], v[188:189], v[202:203]
	v_cvt_pk_f16_f32 v110, v182, v183
	v_cvt_pk_f16_f32 v111, v184, v185
	v_cvt_pk_f16_f32 v112, v186, v187
	v_cvt_pk_f16_f32 v113, v188, v189
	global_store_dwordx4 v[236:237], v[110:113], off sc1
	v_cvt_f32_f16_e32 v182, v150
	v_cvt_f32_f16_sdwa v183, v150 dst_sel:DWORD dst_unused:UNUSED_PAD src0_sel:WORD_1
	v_cvt_f32_f16_e32 v184, v151
	v_cvt_f32_f16_sdwa v185, v151 dst_sel:DWORD dst_unused:UNUSED_PAD src0_sel:WORD_1
	v_cvt_f32_f16_e32 v186, v152
	v_cvt_f32_f16_sdwa v187, v152 dst_sel:DWORD dst_unused:UNUSED_PAD src0_sel:WORD_1
	v_cvt_f32_f16_e32 v188, v153
	v_cvt_f32_f16_sdwa v189, v153 dst_sel:DWORD dst_unused:UNUSED_PAD src0_sel:WORD_1
	v_cvt_f32_f16_e32 v196, v158
	v_cvt_f32_f16_sdwa v197, v158 dst_sel:DWORD dst_unused:UNUSED_PAD src0_sel:WORD_1
	v_cvt_f32_f16_e32 v198, v159
	v_cvt_f32_f16_sdwa v199, v159 dst_sel:DWORD dst_unused:UNUSED_PAD src0_sel:WORD_1
	v_cvt_f32_f16_e32 v200, v160
	v_cvt_f32_f16_sdwa v201, v160 dst_sel:DWORD dst_unused:UNUSED_PAD src0_sel:WORD_1
	v_cvt_f32_f16_e32 v202, v161
	v_cvt_f32_f16_sdwa v203, v161 dst_sel:DWORD dst_unused:UNUSED_PAD src0_sel:WORD_1
	v_pk_mul_f32 v[182:183], v[102:103], v[182:183]
	v_pk_mul_f32 v[184:185], v[104:105], v[184:185]
	v_pk_mul_f32 v[186:187], v[98:99], v[186:187]
	v_pk_mul_f32 v[188:189], v[100:101], v[188:189]
	v_pk_add_f32 v[182:183], v[182:183], v[196:197]
	v_pk_add_f32 v[184:185], v[184:185], v[198:199]
	v_pk_add_f32 v[186:187], v[186:187], v[200:201]
	v_pk_add_f32 v[188:189], v[188:189], v[202:203]
	v_cvt_pk_f16_f32 v102, v182, v183
	v_cvt_pk_f16_f32 v103, v184, v185
	v_cvt_pk_f16_f32 v104, v186, v187
	v_cvt_pk_f16_f32 v105, v188, v189
	global_store_dwordx4 v[236:237], v[102:105], off offset:256 sc1
	v_add_u32_e32 v238, 128, v176
	v_mad_i64_i32 v[234:235], s[0:1], v238, s91, v[174:175]
	v_lshlrev_b32_e32 v240, 11, v238
	v_lshl_add_u64 v[236:237], v[180:181], 0, v[240:241]
	global_load_dwordx4 v[146:149], v[234:235], off
	global_load_dwordx4 v[154:157], v[236:237], off
	global_load_dwordx4 v[150:153], v[234:235], off offset:256
	global_load_dwordx4 v[158:161], v[236:237], off offset:256
	s_nop 1
	v_add_u32_e32 v238, 144, v176
	v_mad_i64_i32 v[234:235], s[0:1], v238, s91, v[174:175]
	v_lshlrev_b32_e32 v240, 11, v238
	v_lshl_add_u64 v[236:237], v[180:181], 0, v[240:241]
	global_load_dwordx4 v[110:113], v[234:235], off
	global_load_dwordx4 v[102:105], v[236:237], off
	global_load_dwordx4 v[106:109], v[234:235], off offset:256
	global_load_dwordx4 v[98:101], v[236:237], off offset:256
	s_waitcnt vmcnt(14)
	v_add_u32_e32 v238, 32, v176
	v_lshlrev_b32_e32 v240, 11, v238
	v_lshl_add_u64 v[236:237], v[180:181], 0, v[240:241]
	v_cvt_f32_f16_e32 v182, v130
	v_cvt_f32_f16_sdwa v183, v130 dst_sel:DWORD dst_unused:UNUSED_PAD src0_sel:WORD_1
	v_cvt_f32_f16_e32 v184, v131
	v_cvt_f32_f16_sdwa v185, v131 dst_sel:DWORD dst_unused:UNUSED_PAD src0_sel:WORD_1
	v_cvt_f32_f16_e32 v186, v132
	v_cvt_f32_f16_sdwa v187, v132 dst_sel:DWORD dst_unused:UNUSED_PAD src0_sel:WORD_1
	v_cvt_f32_f16_e32 v188, v133
	v_cvt_f32_f16_sdwa v189, v133 dst_sel:DWORD dst_unused:UNUSED_PAD src0_sel:WORD_1
	v_cvt_f32_f16_e32 v196, v138
	v_cvt_f32_f16_sdwa v197, v138 dst_sel:DWORD dst_unused:UNUSED_PAD src0_sel:WORD_1
	v_cvt_f32_f16_e32 v198, v139
	v_cvt_f32_f16_sdwa v199, v139 dst_sel:DWORD dst_unused:UNUSED_PAD src0_sel:WORD_1
	v_cvt_f32_f16_e32 v200, v140
	v_cvt_f32_f16_sdwa v201, v140 dst_sel:DWORD dst_unused:UNUSED_PAD src0_sel:WORD_1
	v_cvt_f32_f16_e32 v202, v141
	v_cvt_f32_f16_sdwa v203, v141 dst_sel:DWORD dst_unused:UNUSED_PAD src0_sel:WORD_1
	v_pk_mul_f32 v[182:183], v[92:93], v[182:183]
	v_pk_mul_f32 v[184:185], v[94:95], v[184:185]
	v_pk_mul_f32 v[186:187], v[88:89], v[186:187]
	v_pk_mul_f32 v[188:189], v[90:91], v[188:189]
	v_pk_add_f32 v[182:183], v[182:183], v[196:197]
	v_pk_add_f32 v[184:185], v[184:185], v[198:199]
	v_pk_add_f32 v[186:187], v[186:187], v[200:201]
	v_pk_add_f32 v[188:189], v[188:189], v[202:203]
	v_cvt_pk_f16_f32 v92, v182, v183
	v_cvt_pk_f16_f32 v93, v184, v185
	v_cvt_pk_f16_f32 v94, v186, v187
	v_cvt_pk_f16_f32 v95, v188, v189
	global_store_dwordx4 v[236:237], v[92:95], off sc1
	v_cvt_f32_f16_e32 v182, v134
	v_cvt_f32_f16_sdwa v183, v134 dst_sel:DWORD dst_unused:UNUSED_PAD src0_sel:WORD_1
; __device__ __forceinline__ unsigned cvt_pk_f16(float lo, float hi) { f32x2 v = {lo, hi}; h16x2 b = __builtin_convertvector(v, h16x2); return __builtin_bit_cast(unsigned, b); }
;     __device__ __forceinline__ void operator()(const f32x4 (&acc)[2][2][4][2], const Unit& u, int wr, int wc, int fr, int fq) const {
;     ...
;         } else {
; #pragma unroll
;             for (int ai = 0; ai < 2; ++ai)
; #pragma unroll
;                 for (int mp = 0; mp < 2; ++mp) {
;                     h16x8 gv[2][2], pv[2][2];
; #pragma unroll
;                     for (int mm = 0; mm < 2; ++mm)
; #pragma unroll
;                         for (int bj = 0; bj < 2; ++bj) { const size_t row = (size_t)(row0 + ai * HALF + (2 * mp + mm) * 16);
;                             gv[mm][bj] = *(const h16x8*)(Gn + row * ldg + bj * HALF);
;                             if (n > 0) pv[mm][bj] = *(const h16x8*)(Mg + row * 1024 + col0 + bj * HALF); }
; #pragma unroll
;                     for (int mm = 0; mm < 2; ++mm)
; #pragma unroll
;                         for (int bj = 0; bj < 2; ++bj) { const int m = 2 * mp + mm; const size_t row = (size_t)(row0 + ai * HALF + m * 16);
;                             float o[8];
; #pragma unroll
;                             for (int e = 0; e < 8; ++e) { const float a = e < 4 ? acc[ai][bj][m][0][e] : acc[ai][bj][m][1][e - 4]; o[e] = a * (float)gv[mm][bj][e]; }
;                             if (n > 0) {
; #pragma unroll
;                                 for (int e = 0; e < 8; ++e) o[e] += (float)pv[mm][bj][e]; }
;                             u32x4 w; w.x = cvt_pk_f16(o[0], o[1]); w.y = cvt_pk_f16(o[2], o[3]); w.z = cvt_pk_f16(o[4], o[5]); w.w = cvt_pk_f16(o[6], o[7]);
;                             *(u32x4*)(Mg + row * 1024 + col0 + bj * HALF) = w; }
;                 }
	v_cvt_f32_f16_e32 v184, v135
	v_cvt_f32_f16_sdwa v185, v135 dst_sel:DWORD dst_unused:UNUSED_PAD src0_sel:WORD_1
	v_cvt_f32_f16_e32 v186, v136
	v_cvt_f32_f16_sdwa v187, v136 dst_sel:DWORD dst_unused:UNUSED_PAD src0_sel:WORD_1
	v_cvt_f32_f16_e32 v188, v137
	v_cvt_f32_f16_sdwa v189, v137 dst_sel:DWORD dst_unused:UNUSED_PAD src0_sel:WORD_1
	v_cvt_f32_f16_e32 v196, v142
	v_cvt_f32_f16_sdwa v197, v142 dst_sel:DWORD dst_unused:UNUSED_PAD src0_sel:WORD_1
	v_cvt_f32_f16_e32 v198, v143
	v_cvt_f32_f16_sdwa v199, v143 dst_sel:DWORD dst_unused:UNUSED_PAD src0_sel:WORD_1
	v_cvt_f32_f16_e32 v200, v144
	v_cvt_f32_f16_sdwa v201, v144 dst_sel:DWORD dst_unused:UNUSED_PAD src0_sel:WORD_1
	v_cvt_f32_f16_e32 v202, v145
	v_cvt_f32_f16_sdwa v203, v145 dst_sel:DWORD dst_unused:UNUSED_PAD src0_sel:WORD_1
	v_pk_mul_f32 v[182:183], v[84:85], v[182:183]
	v_pk_mul_f32 v[184:185], v[86:87], v[184:185]
	v_pk_mul_f32 v[186:187], v[80:81], v[186:187]
	v_pk_mul_f32 v[188:189], v[82:83], v[188:189]
	v_pk_add_f32 v[182:183], v[182:183], v[196:197]
	v_pk_add_f32 v[184:185], v[184:185], v[198:199]
	v_pk_add_f32 v[186:187], v[186:187], v[200:201]
	v_pk_add_f32 v[188:189], v[188:189], v[202:203]
	v_cvt_pk_f16_f32 v84, v182, v183
	v_cvt_pk_f16_f32 v85, v184, v185
	v_cvt_pk_f16_f32 v86, v186, v187
	v_cvt_pk_f16_f32 v87, v188, v189
	global_store_dwordx4 v[236:237], v[84:87], off offset:256 sc1
	v_add_u32_e32 v238, 160, v176
	v_mad_i64_i32 v[234:235], s[0:1], v238, s91, v[174:175]
	v_lshlrev_b32_e32 v240, 11, v238
	v_lshl_add_u64 v[236:237], v[180:181], 0, v[240:241]
	global_load_dwordx4 v[130:133], v[234:235], off
	global_load_dwordx4 v[138:141], v[236:237], off
	global_load_dwordx4 v[134:137], v[234:235], off offset:256
	global_load_dwordx4 v[142:145], v[236:237], off offset:256
	s_nop 1
	v_add_u32_e32 v238, 176, v176
	v_mad_i64_i32 v[234:235], s[0:1], v238, s91, v[174:175]
	v_lshlrev_b32_e32 v240, 11, v238
	v_lshl_add_u64 v[236:237], v[180:181], 0, v[240:241]
	global_load_dwordx4 v[92:95], v[234:235], off
	global_load_dwordx4 v[84:87], v[236:237], off
	global_load_dwordx4 v[88:91], v[234:235], off offset:256
	global_load_dwordx4 v[80:83], v[236:237], off offset:256
	s_waitcnt vmcnt(20)
	v_add_u32_e32 v238, 48, v176
	v_lshlrev_b32_e32 v240, 11, v238
	v_lshl_add_u64 v[236:237], v[180:181], 0, v[240:241]
	v_cvt_f32_f16_e32 v182, v126
	v_cvt_f32_f16_sdwa v183, v126 dst_sel:DWORD dst_unused:UNUSED_PAD src0_sel:WORD_1
	v_cvt_f32_f16_e32 v184, v127
	v_cvt_f32_f16_sdwa v185, v127 dst_sel:DWORD dst_unused:UNUSED_PAD src0_sel:WORD_1
	v_cvt_f32_f16_e32 v186, v128
	v_cvt_f32_f16_sdwa v187, v128 dst_sel:DWORD dst_unused:UNUSED_PAD src0_sel:WORD_1
	v_cvt_f32_f16_e32 v188, v129
	v_cvt_f32_f16_sdwa v189, v129 dst_sel:DWORD dst_unused:UNUSED_PAD src0_sel:WORD_1
	v_cvt_f32_f16_e32 v196, v118
	v_cvt_f32_f16_sdwa v197, v118 dst_sel:DWORD dst_unused:UNUSED_PAD src0_sel:WORD_1
	v_cvt_f32_f16_e32 v198, v119
	v_cvt_f32_f16_sdwa v199, v119 dst_sel:DWORD dst_unused:UNUSED_PAD src0_sel:WORD_1
	v_cvt_f32_f16_e32 v200, v120
	v_cvt_f32_f16_sdwa v201, v120 dst_sel:DWORD dst_unused:UNUSED_PAD src0_sel:WORD_1
	v_cvt_f32_f16_e32 v202, v121
	v_cvt_f32_f16_sdwa v203, v121 dst_sel:DWORD dst_unused:UNUSED_PAD src0_sel:WORD_1
	v_pk_mul_f32 v[182:183], v[76:77], v[182:183]
	v_pk_mul_f32 v[184:185], v[78:79], v[184:185]
	v_pk_mul_f32 v[186:187], v[72:73], v[186:187]
	v_pk_mul_f32 v[188:189], v[74:75], v[188:189]
	v_pk_add_f32 v[182:183], v[182:183], v[196:197]
	v_pk_add_f32 v[184:185], v[184:185], v[198:199]
	v_pk_add_f32 v[186:187], v[186:187], v[200:201]
	v_pk_add_f32 v[188:189], v[188:189], v[202:203]
	v_cvt_pk_f16_f32 v76, v182, v183
	v_cvt_pk_f16_f32 v77, v184, v185
	v_cvt_pk_f16_f32 v78, v186, v187
	v_cvt_pk_f16_f32 v79, v188, v189
	global_store_dwordx4 v[236:237], v[76:79], off sc1
	v_cvt_f32_f16_e32 v182, v122
	v_cvt_f32_f16_sdwa v183, v122 dst_sel:DWORD dst_unused:UNUSED_PAD src0_sel:WORD_1
	v_cvt_f32_f16_e32 v184, v123
	v_cvt_f32_f16_sdwa v185, v123 dst_sel:DWORD dst_unused:UNUSED_PAD src0_sel:WORD_1
	v_cvt_f32_f16_e32 v186, v124
	v_cvt_f32_f16_sdwa v187, v124 dst_sel:DWORD dst_unused:UNUSED_PAD src0_sel:WORD_1
	v_cvt_f32_f16_e32 v188, v125
	v_cvt_f32_f16_sdwa v189, v125 dst_sel:DWORD dst_unused:UNUSED_PAD src0_sel:WORD_1
	v_cvt_f32_f16_e32 v196, v114
	v_cvt_f32_f16_sdwa v197, v114 dst_sel:DWORD dst_unused:UNUSED_PAD src0_sel:WORD_1
	v_cvt_f32_f16_e32 v198, v115
	v_cvt_f32_f16_sdwa v199, v115 dst_sel:DWORD dst_unused:UNUSED_PAD src0_sel:WORD_1
	v_cvt_f32_f16_e32 v200, v116
	v_cvt_f32_f16_sdwa v201, v116 dst_sel:DWORD dst_unused:UNUSED_PAD src0_sel:WORD_1
	v_cvt_f32_f16_e32 v202, v117
	v_cvt_f32_f16_sdwa v203, v117 dst_sel:DWORD dst_unused:UNUSED_PAD src0_sel:WORD_1
	v_pk_mul_f32 v[182:183], v[68:69], v[182:183]
	v_pk_mul_f32 v[184:185], v[70:71], v[184:185]
	v_pk_mul_f32 v[186:187], v[64:65], v[186:187]
	v_pk_mul_f32 v[188:189], v[66:67], v[188:189]
	v_pk_add_f32 v[182:183], v[182:183], v[196:197]
	v_pk_add_f32 v[184:185], v[184:185], v[198:199]
	v_pk_add_f32 v[186:187], v[186:187], v[200:201]
	v_pk_add_f32 v[188:189], v[188:189], v[202:203]
	v_cvt_pk_f16_f32 v68, v182, v183
	v_cvt_pk_f16_f32 v69, v184, v185
	v_cvt_pk_f16_f32 v70, v186, v187
	v_cvt_pk_f16_f32 v71, v188, v189
	global_store_dwordx4 v[236:237], v[68:71], off offset:256 sc1
	s_waitcnt vmcnt(16)
; __device__ __forceinline__ unsigned cvt_pk_f16(float lo, float hi) { f32x2 v = {lo, hi}; h16x2 b = __builtin_convertvector(v, h16x2); return __builtin_bit_cast(unsigned, b); }
;     __device__ __forceinline__ void operator()(const f32x4 (&acc)[2][2][4][2], const Unit& u, int wr, int wc, int fr, int fq) const {
;     ...
;         } else {
; #pragma unroll
;             for (int ai = 0; ai < 2; ++ai)
; #pragma unroll
;                 for (int mp = 0; mp < 2; ++mp) {
;                     h16x8 gv[2][2], pv[2][2];
; #pragma unroll
;                     for (int mm = 0; mm < 2; ++mm)
; #pragma unroll
;                         for (int bj = 0; bj < 2; ++bj) { const size_t row = (size_t)(row0 + ai * HALF + (2 * mp + mm) * 16);
;                             gv[mm][bj] = *(const h16x8*)(Gn + row * ldg + bj * HALF);
;                             if (n > 0) pv[mm][bj] = *(const h16x8*)(Mg + row * 1024 + col0 + bj * HALF); }
; #pragma unroll
;                     for (int mm = 0; mm < 2; ++mm)
; #pragma unroll
;                         for (int bj = 0; bj < 2; ++bj) { const int m = 2 * mp + mm; const size_t row = (size_t)(row0 + ai * HALF + m * 16);
;                             float o[8];
; #pragma unroll
;                             for (int e = 0; e < 8; ++e) { const float a = e < 4 ? acc[ai][bj][m][0][e] : acc[ai][bj][m][1][e - 4]; o[e] = a * (float)gv[mm][bj][e]; }
;                             if (n > 0) {
; #pragma unroll
;                                 for (int e = 0; e < 8; ++e) o[e] += (float)pv[mm][bj][e]; }
;                             u32x4 w; w.x = cvt_pk_f16(o[0], o[1]); w.y = cvt_pk_f16(o[2], o[3]); w.z = cvt_pk_f16(o[4], o[5]); w.w = cvt_pk_f16(o[6], o[7]);
;                             *(u32x4*)(Mg + row * 1024 + col0 + bj * HALF) = w; }
;                 }
	v_add_u32_e32 v238, 128, v176
	v_lshlrev_b32_e32 v240, 11, v238
	v_lshl_add_u64 v[236:237], v[180:181], 0, v[240:241]
	v_cvt_f32_f16_e32 v182, v146
	v_cvt_f32_f16_sdwa v183, v146 dst_sel:DWORD dst_unused:UNUSED_PAD src0_sel:WORD_1
	v_cvt_f32_f16_e32 v184, v147
	v_cvt_f32_f16_sdwa v185, v147 dst_sel:DWORD dst_unused:UNUSED_PAD src0_sel:WORD_1
	v_cvt_f32_f16_e32 v186, v148
	v_cvt_f32_f16_sdwa v187, v148 dst_sel:DWORD dst_unused:UNUSED_PAD src0_sel:WORD_1
	v_cvt_f32_f16_e32 v188, v149
	v_cvt_f32_f16_sdwa v189, v149 dst_sel:DWORD dst_unused:UNUSED_PAD src0_sel:WORD_1
	v_cvt_f32_f16_e32 v196, v154
	v_cvt_f32_f16_sdwa v197, v154 dst_sel:DWORD dst_unused:UNUSED_PAD src0_sel:WORD_1
	v_cvt_f32_f16_e32 v198, v155
	v_cvt_f32_f16_sdwa v199, v155 dst_sel:DWORD dst_unused:UNUSED_PAD src0_sel:WORD_1
	v_cvt_f32_f16_e32 v200, v156
	v_cvt_f32_f16_sdwa v201, v156 dst_sel:DWORD dst_unused:UNUSED_PAD src0_sel:WORD_1
	v_cvt_f32_f16_e32 v202, v157
	v_cvt_f32_f16_sdwa v203, v157 dst_sel:DWORD dst_unused:UNUSED_PAD src0_sel:WORD_1
	v_pk_mul_f32 v[182:183], v[60:61], v[182:183]
	v_pk_mul_f32 v[184:185], v[62:63], v[184:185]
	v_pk_mul_f32 v[186:187], v[56:57], v[186:187]
	v_pk_mul_f32 v[188:189], v[58:59], v[188:189]
	v_pk_add_f32 v[182:183], v[182:183], v[196:197]
	v_pk_add_f32 v[184:185], v[184:185], v[198:199]
	v_pk_add_f32 v[186:187], v[186:187], v[200:201]
	v_pk_add_f32 v[188:189], v[188:189], v[202:203]
	v_cvt_pk_f16_f32 v60, v182, v183
	v_cvt_pk_f16_f32 v61, v184, v185
	v_cvt_pk_f16_f32 v62, v186, v187
	v_cvt_pk_f16_f32 v63, v188, v189
	global_store_dwordx4 v[236:237], v[60:63], off sc1
	v_cvt_f32_f16_e32 v182, v150
	v_cvt_f32_f16_sdwa v183, v150 dst_sel:DWORD dst_unused:UNUSED_PAD src0_sel:WORD_1
	v_cvt_f32_f16_e32 v184, v151
	v_cvt_f32_f16_sdwa v185, v151 dst_sel:DWORD dst_unused:UNUSED_PAD src0_sel:WORD_1
	v_cvt_f32_f16_e32 v186, v152
	v_cvt_f32_f16_sdwa v187, v152 dst_sel:DWORD dst_unused:UNUSED_PAD src0_sel:WORD_1
	v_cvt_f32_f16_e32 v188, v153
	v_cvt_f32_f16_sdwa v189, v153 dst_sel:DWORD dst_unused:UNUSED_PAD src0_sel:WORD_1
	v_cvt_f32_f16_e32 v196, v158
	v_cvt_f32_f16_sdwa v197, v158 dst_sel:DWORD dst_unused:UNUSED_PAD src0_sel:WORD_1
	v_cvt_f32_f16_e32 v198, v159
	v_cvt_f32_f16_sdwa v199, v159 dst_sel:DWORD dst_unused:UNUSED_PAD src0_sel:WORD_1
	v_cvt_f32_f16_e32 v200, v160
	v_cvt_f32_f16_sdwa v201, v160 dst_sel:DWORD dst_unused:UNUSED_PAD src0_sel:WORD_1
	v_cvt_f32_f16_e32 v202, v161
	v_cvt_f32_f16_sdwa v203, v161 dst_sel:DWORD dst_unused:UNUSED_PAD src0_sel:WORD_1
	v_pk_mul_f32 v[182:183], v[52:53], v[182:183]
	v_pk_mul_f32 v[184:185], v[54:55], v[184:185]
	v_pk_mul_f32 v[186:187], v[48:49], v[186:187]
	v_pk_mul_f32 v[188:189], v[50:51], v[188:189]
	v_pk_add_f32 v[182:183], v[182:183], v[196:197]
	v_pk_add_f32 v[184:185], v[184:185], v[198:199]
	v_pk_add_f32 v[186:187], v[186:187], v[200:201]
	v_pk_add_f32 v[188:189], v[188:189], v[202:203]
	v_cvt_pk_f16_f32 v52, v182, v183
	v_cvt_pk_f16_f32 v53, v184, v185
	v_cvt_pk_f16_f32 v54, v186, v187
	v_cvt_pk_f16_f32 v55, v188, v189
	global_store_dwordx4 v[236:237], v[52:55], off offset:256 sc1
	s_waitcnt vmcnt(14)
	v_add_u32_e32 v238, 144, v176
	v_lshlrev_b32_e32 v240, 11, v238
	v_lshl_add_u64 v[236:237], v[180:181], 0, v[240:241]
	v_cvt_f32_f16_e32 v182, v110
	v_cvt_f32_f16_sdwa v183, v110 dst_sel:DWORD dst_unused:UNUSED_PAD src0_sel:WORD_1
	v_cvt_f32_f16_e32 v184, v111
	v_cvt_f32_f16_sdwa v185, v111 dst_sel:DWORD dst_unused:UNUSED_PAD src0_sel:WORD_1
	v_cvt_f32_f16_e32 v186, v112
	v_cvt_f32_f16_sdwa v187, v112 dst_sel:DWORD dst_unused:UNUSED_PAD src0_sel:WORD_1
	v_cvt_f32_f16_e32 v188, v113
	v_cvt_f32_f16_sdwa v189, v113 dst_sel:DWORD dst_unused:UNUSED_PAD src0_sel:WORD_1
	v_cvt_f32_f16_e32 v196, v102
	v_cvt_f32_f16_sdwa v197, v102 dst_sel:DWORD dst_unused:UNUSED_PAD src0_sel:WORD_1
	v_cvt_f32_f16_e32 v198, v103
	v_cvt_f32_f16_sdwa v199, v103 dst_sel:DWORD dst_unused:UNUSED_PAD src0_sel:WORD_1
	v_cvt_f32_f16_e32 v200, v104
	v_cvt_f32_f16_sdwa v201, v104 dst_sel:DWORD dst_unused:UNUSED_PAD src0_sel:WORD_1
	v_cvt_f32_f16_e32 v202, v105
	v_cvt_f32_f16_sdwa v203, v105 dst_sel:DWORD dst_unused:UNUSED_PAD src0_sel:WORD_1
	v_pk_mul_f32 v[182:183], v[44:45], v[182:183]
	v_pk_mul_f32 v[184:185], v[46:47], v[184:185]
	v_pk_mul_f32 v[186:187], v[40:41], v[186:187]
	v_pk_mul_f32 v[188:189], v[42:43], v[188:189]
	v_pk_add_f32 v[182:183], v[182:183], v[196:197]
	v_pk_add_f32 v[184:185], v[184:185], v[198:199]
	v_pk_add_f32 v[186:187], v[186:187], v[200:201]
	v_pk_add_f32 v[188:189], v[188:189], v[202:203]
	v_cvt_pk_f16_f32 v44, v182, v183
	v_cvt_pk_f16_f32 v45, v184, v185
	v_cvt_pk_f16_f32 v46, v186, v187
	v_cvt_pk_f16_f32 v47, v188, v189
	global_store_dwordx4 v[236:237], v[44:47], off sc1
	v_cvt_f32_f16_e32 v182, v106
	v_cvt_f32_f16_sdwa v183, v106 dst_sel:DWORD dst_unused:UNUSED_PAD src0_sel:WORD_1
	v_cvt_f32_f16_e32 v184, v107
	v_cvt_f32_f16_sdwa v185, v107 dst_sel:DWORD dst_unused:UNUSED_PAD src0_sel:WORD_1
	v_cvt_f32_f16_e32 v186, v108
	v_cvt_f32_f16_sdwa v187, v108 dst_sel:DWORD dst_unused:UNUSED_PAD src0_sel:WORD_1
	v_cvt_f32_f16_e32 v188, v109
	v_cvt_f32_f16_sdwa v189, v109 dst_sel:DWORD dst_unused:UNUSED_PAD src0_sel:WORD_1
	v_cvt_f32_f16_e32 v196, v98
	v_cvt_f32_f16_sdwa v197, v98 dst_sel:DWORD dst_unused:UNUSED_PAD src0_sel:WORD_1
	v_cvt_f32_f16_e32 v198, v99
	v_cvt_f32_f16_sdwa v199, v99 dst_sel:DWORD dst_unused:UNUSED_PAD src0_sel:WORD_1
	v_cvt_f32_f16_e32 v200, v100
	v_cvt_f32_f16_sdwa v201, v100 dst_sel:DWORD dst_unused:UNUSED_PAD src0_sel:WORD_1
	v_cvt_f32_f16_e32 v202, v101
	v_cvt_f32_f16_sdwa v203, v101 dst_sel:DWORD dst_unused:UNUSED_PAD src0_sel:WORD_1
	v_pk_mul_f32 v[182:183], v[28:29], v[182:183]
	v_pk_mul_f32 v[184:185], v[30:31], v[184:185]
	v_pk_mul_f32 v[186:187], v[24:25], v[186:187]
	v_pk_mul_f32 v[188:189], v[26:27], v[188:189]
	v_pk_add_f32 v[182:183], v[182:183], v[196:197]
	v_pk_add_f32 v[184:185], v[184:185], v[198:199]
	v_pk_add_f32 v[186:187], v[186:187], v[200:201]
	v_pk_add_f32 v[188:189], v[188:189], v[202:203]
	v_cvt_pk_f16_f32 v28, v182, v183
	v_cvt_pk_f16_f32 v29, v184, v185
	v_cvt_pk_f16_f32 v30, v186, v187
	v_cvt_pk_f16_f32 v31, v188, v189
	global_store_dwordx4 v[236:237], v[28:31], off offset:256 sc1
	s_waitcnt vmcnt(10)
; __device__ __forceinline__ unsigned cvt_pk_f16(float lo, float hi) { f32x2 v = {lo, hi}; h16x2 b = __builtin_convertvector(v, h16x2); return __builtin_bit_cast(unsigned, b); }
;     __device__ __forceinline__ void operator()(const f32x4 (&acc)[2][2][4][2], const Unit& u, int wr, int wc, int fr, int fq) const {
;     ...
;         } else {
; #pragma unroll
;             for (int ai = 0; ai < 2; ++ai)
; #pragma unroll
;                 for (int mp = 0; mp < 2; ++mp) {
;                     h16x8 gv[2][2], pv[2][2];
; #pragma unroll
;                     for (int mm = 0; mm < 2; ++mm)
; #pragma unroll
;                         for (int bj = 0; bj < 2; ++bj) { const size_t row = (size_t)(row0 + ai * HALF + (2 * mp + mm) * 16);
;                             gv[mm][bj] = *(const h16x8*)(Gn + row * ldg + bj * HALF);
;                             if (n > 0) pv[mm][bj] = *(const h16x8*)(Mg + row * 1024 + col0 + bj * HALF); }
; #pragma unroll
;                     for (int mm = 0; mm < 2; ++mm)
; #pragma unroll
;                         for (int bj = 0; bj < 2; ++bj) { const int m = 2 * mp + mm; const size_t row = (size_t)(row0 + ai * HALF + m * 16);
;                             float o[8];
; #pragma unroll
;                             for (int e = 0; e < 8; ++e) { const float a = e < 4 ? acc[ai][bj][m][0][e] : acc[ai][bj][m][1][e - 4]; o[e] = a * (float)gv[mm][bj][e]; }
;                             if (n > 0) {
; #pragma unroll
;                                 for (int e = 0; e < 8; ++e) o[e] += (float)pv[mm][bj][e]; }
;                             u32x4 w; w.x = cvt_pk_f16(o[0], o[1]); w.y = cvt_pk_f16(o[2], o[3]); w.z = cvt_pk_f16(o[4], o[5]); w.w = cvt_pk_f16(o[6], o[7]);
;                             *(u32x4*)(Mg + row * 1024 + col0 + bj * HALF) = w; }
;                 }
	v_add_u32_e32 v238, 160, v176
	v_lshlrev_b32_e32 v240, 11, v238
	v_lshl_add_u64 v[236:237], v[180:181], 0, v[240:241]
	v_cvt_f32_f16_e32 v182, v130
	v_cvt_f32_f16_sdwa v183, v130 dst_sel:DWORD dst_unused:UNUSED_PAD src0_sel:WORD_1
	v_cvt_f32_f16_e32 v184, v131
	v_cvt_f32_f16_sdwa v185, v131 dst_sel:DWORD dst_unused:UNUSED_PAD src0_sel:WORD_1
	v_cvt_f32_f16_e32 v186, v132
	v_cvt_f32_f16_sdwa v187, v132 dst_sel:DWORD dst_unused:UNUSED_PAD src0_sel:WORD_1
	v_cvt_f32_f16_e32 v188, v133
	v_cvt_f32_f16_sdwa v189, v133 dst_sel:DWORD dst_unused:UNUSED_PAD src0_sel:WORD_1
	v_cvt_f32_f16_e32 v196, v138
	v_cvt_f32_f16_sdwa v197, v138 dst_sel:DWORD dst_unused:UNUSED_PAD src0_sel:WORD_1
	v_cvt_f32_f16_e32 v198, v139
	v_cvt_f32_f16_sdwa v199, v139 dst_sel:DWORD dst_unused:UNUSED_PAD src0_sel:WORD_1
	v_cvt_f32_f16_e32 v200, v140
	v_cvt_f32_f16_sdwa v201, v140 dst_sel:DWORD dst_unused:UNUSED_PAD src0_sel:WORD_1
	v_cvt_f32_f16_e32 v202, v141
	v_cvt_f32_f16_sdwa v203, v141 dst_sel:DWORD dst_unused:UNUSED_PAD src0_sel:WORD_1
	v_pk_mul_f32 v[182:183], v[20:21], v[182:183]
	v_pk_mul_f32 v[184:185], v[22:23], v[184:185]
	v_pk_mul_f32 v[186:187], v[16:17], v[186:187]
	v_pk_mul_f32 v[188:189], v[18:19], v[188:189]
	v_pk_add_f32 v[182:183], v[182:183], v[196:197]
	v_pk_add_f32 v[184:185], v[184:185], v[198:199]
	v_pk_add_f32 v[186:187], v[186:187], v[200:201]
	v_pk_add_f32 v[188:189], v[188:189], v[202:203]
	v_cvt_pk_f16_f32 v20, v182, v183
	v_cvt_pk_f16_f32 v21, v184, v185
	v_cvt_pk_f16_f32 v22, v186, v187
	v_cvt_pk_f16_f32 v23, v188, v189
	global_store_dwordx4 v[236:237], v[20:23], off sc1
	v_cvt_f32_f16_e32 v182, v134
	v_cvt_f32_f16_sdwa v183, v134 dst_sel:DWORD dst_unused:UNUSED_PAD src0_sel:WORD_1
	v_cvt_f32_f16_e32 v184, v135
	v_cvt_f32_f16_sdwa v185, v135 dst_sel:DWORD dst_unused:UNUSED_PAD src0_sel:WORD_1
	v_cvt_f32_f16_e32 v186, v136
	v_cvt_f32_f16_sdwa v187, v136 dst_sel:DWORD dst_unused:UNUSED_PAD src0_sel:WORD_1
	v_cvt_f32_f16_e32 v188, v137
	v_cvt_f32_f16_sdwa v189, v137 dst_sel:DWORD dst_unused:UNUSED_PAD src0_sel:WORD_1
	v_cvt_f32_f16_e32 v196, v142
	v_cvt_f32_f16_sdwa v197, v142 dst_sel:DWORD dst_unused:UNUSED_PAD src0_sel:WORD_1
	v_cvt_f32_f16_e32 v198, v143
	v_cvt_f32_f16_sdwa v199, v143 dst_sel:DWORD dst_unused:UNUSED_PAD src0_sel:WORD_1
	v_cvt_f32_f16_e32 v200, v144
	v_cvt_f32_f16_sdwa v201, v144 dst_sel:DWORD dst_unused:UNUSED_PAD src0_sel:WORD_1
	v_cvt_f32_f16_e32 v202, v145
	v_cvt_f32_f16_sdwa v203, v145 dst_sel:DWORD dst_unused:UNUSED_PAD src0_sel:WORD_1
	v_pk_mul_f32 v[182:183], v[32:33], v[182:183]
	v_pk_mul_f32 v[184:185], v[34:35], v[184:185]
	v_pk_mul_f32 v[186:187], v[36:37], v[186:187]
	v_pk_mul_f32 v[188:189], v[38:39], v[188:189]
	v_pk_add_f32 v[182:183], v[182:183], v[196:197]
	v_pk_add_f32 v[184:185], v[184:185], v[198:199]
	v_pk_add_f32 v[186:187], v[186:187], v[200:201]
	v_pk_add_f32 v[188:189], v[188:189], v[202:203]
	v_cvt_pk_f16_f32 v32, v182, v183
	v_cvt_pk_f16_f32 v33, v184, v185
	v_cvt_pk_f16_f32 v34, v186, v187
	v_cvt_pk_f16_f32 v35, v188, v189
	global_store_dwordx4 v[236:237], v[32:35], off offset:256 sc1
	s_waitcnt vmcnt(8)
	v_add_u32_e32 v238, 176, v176
	v_lshlrev_b32_e32 v240, 11, v238
	v_lshl_add_u64 v[236:237], v[180:181], 0, v[240:241]
	v_cvt_f32_f16_e32 v182, v92
	v_cvt_f32_f16_sdwa v183, v92 dst_sel:DWORD dst_unused:UNUSED_PAD src0_sel:WORD_1
	v_cvt_f32_f16_e32 v184, v93
	v_cvt_f32_f16_sdwa v185, v93 dst_sel:DWORD dst_unused:UNUSED_PAD src0_sel:WORD_1
	v_cvt_f32_f16_e32 v186, v94
	v_cvt_f32_f16_sdwa v187, v94 dst_sel:DWORD dst_unused:UNUSED_PAD src0_sel:WORD_1
	v_cvt_f32_f16_e32 v188, v95
	v_cvt_f32_f16_sdwa v189, v95 dst_sel:DWORD dst_unused:UNUSED_PAD src0_sel:WORD_1
	v_cvt_f32_f16_e32 v196, v84
	v_cvt_f32_f16_sdwa v197, v84 dst_sel:DWORD dst_unused:UNUSED_PAD src0_sel:WORD_1
	v_cvt_f32_f16_e32 v198, v85
	v_cvt_f32_f16_sdwa v199, v85 dst_sel:DWORD dst_unused:UNUSED_PAD src0_sel:WORD_1
	v_cvt_f32_f16_e32 v200, v86
	v_cvt_f32_f16_sdwa v201, v86 dst_sel:DWORD dst_unused:UNUSED_PAD src0_sel:WORD_1
	v_cvt_f32_f16_e32 v202, v87
	v_cvt_f32_f16_sdwa v203, v87 dst_sel:DWORD dst_unused:UNUSED_PAD src0_sel:WORD_1
	v_pk_mul_f32 v[182:183], v[4:5], v[182:183]
	v_pk_mul_f32 v[184:185], v[6:7], v[184:185]
	v_pk_mul_f32 v[186:187], v[0:1], v[186:187]
	v_pk_mul_f32 v[188:189], v[2:3], v[188:189]
	v_pk_add_f32 v[182:183], v[182:183], v[196:197]
	v_pk_add_f32 v[184:185], v[184:185], v[198:199]
	v_pk_add_f32 v[186:187], v[186:187], v[200:201]
	v_pk_add_f32 v[188:189], v[188:189], v[202:203]
	v_cvt_pk_f16_f32 v4, v182, v183
	v_cvt_pk_f16_f32 v5, v184, v185
	v_cvt_pk_f16_f32 v6, v186, v187
	v_cvt_pk_f16_f32 v7, v188, v189
	global_store_dwordx4 v[236:237], v[4:7], off sc1
	v_cvt_f32_f16_e32 v182, v88
	v_cvt_f32_f16_sdwa v183, v88 dst_sel:DWORD dst_unused:UNUSED_PAD src0_sel:WORD_1
	v_cvt_f32_f16_e32 v184, v89
	v_cvt_f32_f16_sdwa v185, v89 dst_sel:DWORD dst_unused:UNUSED_PAD src0_sel:WORD_1
	v_cvt_f32_f16_e32 v186, v90
	v_cvt_f32_f16_sdwa v187, v90 dst_sel:DWORD dst_unused:UNUSED_PAD src0_sel:WORD_1
	v_cvt_f32_f16_e32 v188, v91
	v_cvt_f32_f16_sdwa v189, v91 dst_sel:DWORD dst_unused:UNUSED_PAD src0_sel:WORD_1
	v_cvt_f32_f16_e32 v196, v80
	v_cvt_f32_f16_sdwa v197, v80 dst_sel:DWORD dst_unused:UNUSED_PAD src0_sel:WORD_1
	v_cvt_f32_f16_e32 v198, v81
	v_cvt_f32_f16_sdwa v199, v81 dst_sel:DWORD dst_unused:UNUSED_PAD src0_sel:WORD_1
	v_cvt_f32_f16_e32 v200, v82
	v_cvt_f32_f16_sdwa v201, v82 dst_sel:DWORD dst_unused:UNUSED_PAD src0_sel:WORD_1
	v_cvt_f32_f16_e32 v202, v83
	v_cvt_f32_f16_sdwa v203, v83 dst_sel:DWORD dst_unused:UNUSED_PAD src0_sel:WORD_1
	v_pk_mul_f32 v[182:183], v[8:9], v[182:183]
	v_pk_mul_f32 v[184:185], v[10:11], v[184:185]
	v_pk_mul_f32 v[186:187], v[12:13], v[186:187]
	v_pk_mul_f32 v[188:189], v[14:15], v[188:189]
	v_pk_add_f32 v[182:183], v[182:183], v[196:197]
	v_pk_add_f32 v[184:185], v[184:185], v[198:199]
	v_pk_add_f32 v[186:187], v[186:187], v[200:201]
	v_pk_add_f32 v[188:189], v[188:189], v[202:203]
	v_cvt_pk_f16_f32 v8, v182, v183
	v_cvt_pk_f16_f32 v9, v184, v185
	v_cvt_pk_f16_f32 v10, v186, v187
	v_cvt_pk_f16_f32 v11, v188, v189
	global_store_dwordx4 v[236:237], v[8:11], off offset:256 sc1
	s_branch .Lbrepi_done
; __device__ __forceinline__ unsigned cvt_pk_f16(float lo, float hi) { f32x2 v = {lo, hi}; h16x2 b = __builtin_convertvector(v, h16x2); return __builtin_bit_cast(unsigned, b); }
;     __device__ __forceinline__ void operator()(const f32x4 (&acc)[2][2][4][2], const Unit& u, int wr, int wc, int fr, int fq) const {
;     ...
;                         for (int bj = 0; bj < 2; ++bj) { const size_t row = (size_t)(row0 + ai * HALF + (2 * mp + mm) * 16);
;                             gv[mm][bj] = *(const h16x8*)(Gn + row * ldg + bj * HALF);
;                             if (n > 0) pv[mm][bj] = *(const h16x8*)(Mg + row * 1024 + col0 + bj * HALF); }
; #pragma unroll
;                     for (int mm = 0; mm < 2; ++mm)
; #pragma unroll
;                         for (int bj = 0; bj < 2; ++bj) { const int m = 2 * mp + mm; const size_t row = (size_t)(row0 + ai * HALF + m * 16);
;                             float o[8];
; #pragma unroll
;                             for (int e = 0; e < 8; ++e) { const float a = e < 4 ? acc[ai][bj][m][0][e] : acc[ai][bj][m][1][e - 4]; o[e] = a * (float)gv[mm][bj][e]; }
;                             if (n > 0) {
; #pragma unroll
;                                 for (int e = 0; e < 8; ++e) o[e] += (float)pv[mm][bj][e]; }
;                             u32x4 w; w.x = cvt_pk_f16(o[0], o[1]); w.y = cvt_pk_f16(o[2], o[3]); w.z = cvt_pk_f16(o[4], o[5]); w.w = cvt_pk_f16(o[6], o[7]);
;                             *(u32x4*)(Mg + row * 1024 + col0 + bj * HALF) = w; }
.Lbrepi_n0:
	v_readlane_b32 s40, v254, 46
	v_readlane_b32 s41, v254, 47
	v_mov_b32_e32 v241, 0
	s_nop 1
	v_lshl_add_u64 v[180:181], v[178:179], 1, s[40:41]
	v_mov_b32_e32 v238, v176
	v_mad_i64_i32 v[234:235], s[0:1], v238, s91, v[174:175]
	global_load_dwordx4 v[130:133], v[234:235], off
	global_load_dwordx4 v[134:137], v[234:235], off offset:256
	v_add_u32_e32 v238, 16, v176
	v_mad_i64_i32 v[234:235], s[0:1], v238, s91, v[174:175]
	global_load_dwordx4 v[146:149], v[234:235], off
	global_load_dwordx4 v[150:153], v[234:235], off offset:256
	s_waitcnt vmcnt(2)
	v_mov_b32_e32 v238, v176
	v_lshlrev_b32_e32 v240, 11, v238
	v_lshl_add_u64 v[236:237], v[180:181], 0, v[240:241]
	v_cvt_f32_f16_e32 v182, v130
	v_cvt_f32_f16_sdwa v183, v130 dst_sel:DWORD dst_unused:UNUSED_PAD src0_sel:WORD_1
	v_cvt_f32_f16_e32 v184, v131
	v_cvt_f32_f16_sdwa v185, v131 dst_sel:DWORD dst_unused:UNUSED_PAD src0_sel:WORD_1
	v_cvt_f32_f16_e32 v186, v132
	v_cvt_f32_f16_sdwa v187, v132 dst_sel:DWORD dst_unused:UNUSED_PAD src0_sel:WORD_1
	v_cvt_f32_f16_e32 v188, v133
	v_cvt_f32_f16_sdwa v189, v133 dst_sel:DWORD dst_unused:UNUSED_PAD src0_sel:WORD_1
	v_pk_mul_f32 v[182:183], v[126:127], v[182:183]
	v_pk_mul_f32 v[184:185], v[128:129], v[184:185]
	v_pk_mul_f32 v[186:187], v[122:123], v[186:187]
	v_pk_mul_f32 v[188:189], v[124:125], v[188:189]
	v_cvt_pk_f16_f32 v126, v182, v183
	v_cvt_pk_f16_f32 v127, v184, v185
	v_cvt_pk_f16_f32 v128, v186, v187
	v_cvt_pk_f16_f32 v129, v188, v189
	global_store_dwordx4 v[236:237], v[126:129], off sc1
	v_cvt_f32_f16_e32 v182, v134
	v_cvt_f32_f16_sdwa v183, v134 dst_sel:DWORD dst_unused:UNUSED_PAD src0_sel:WORD_1
	v_cvt_f32_f16_e32 v184, v135
	v_cvt_f32_f16_sdwa v185, v135 dst_sel:DWORD dst_unused:UNUSED_PAD src0_sel:WORD_1
	v_cvt_f32_f16_e32 v186, v136
	v_cvt_f32_f16_sdwa v187, v136 dst_sel:DWORD dst_unused:UNUSED_PAD src0_sel:WORD_1
	v_cvt_f32_f16_e32 v188, v137
	v_cvt_f32_f16_sdwa v189, v137 dst_sel:DWORD dst_unused:UNUSED_PAD src0_sel:WORD_1
	v_pk_mul_f32 v[182:183], v[118:119], v[182:183]
	v_pk_mul_f32 v[184:185], v[120:121], v[184:185]
	v_pk_mul_f32 v[186:187], v[114:115], v[186:187]
	v_pk_mul_f32 v[188:189], v[116:117], v[188:189]
	v_cvt_pk_f16_f32 v118, v182, v183
	v_cvt_pk_f16_f32 v119, v184, v185
	v_cvt_pk_f16_f32 v120, v186, v187
	v_cvt_pk_f16_f32 v121, v188, v189
	global_store_dwordx4 v[236:237], v[118:121], off offset:256 sc1
	v_add_u32_e32 v238, 32, v176
	v_mad_i64_i32 v[234:235], s[0:1], v238, s91, v[174:175]
	global_load_dwordx4 v[130:133], v[234:235], off
	global_load_dwordx4 v[134:137], v[234:235], off offset:256
	s_nop 1
	v_add_u32_e32 v238, 48, v176
	v_mad_i64_i32 v[234:235], s[0:1], v238, s91, v[174:175]
	global_load_dwordx4 v[126:129], v[234:235], off
	global_load_dwordx4 v[122:125], v[234:235], off offset:256
	s_waitcnt vmcnt(6)
	v_add_u32_e32 v238, 16, v176
	v_lshlrev_b32_e32 v240, 11, v238
	v_lshl_add_u64 v[236:237], v[180:181], 0, v[240:241]
	v_cvt_f32_f16_e32 v182, v146
	v_cvt_f32_f16_sdwa v183, v146 dst_sel:DWORD dst_unused:UNUSED_PAD src0_sel:WORD_1
	v_cvt_f32_f16_e32 v184, v147
	v_cvt_f32_f16_sdwa v185, v147 dst_sel:DWORD dst_unused:UNUSED_PAD src0_sel:WORD_1
	v_cvt_f32_f16_e32 v186, v148
	v_cvt_f32_f16_sdwa v187, v148 dst_sel:DWORD dst_unused:UNUSED_PAD src0_sel:WORD_1
	v_cvt_f32_f16_e32 v188, v149
	v_cvt_f32_f16_sdwa v189, v149 dst_sel:DWORD dst_unused:UNUSED_PAD src0_sel:WORD_1
	v_pk_mul_f32 v[182:183], v[110:111], v[182:183]
	v_pk_mul_f32 v[184:185], v[112:113], v[184:185]
	v_pk_mul_f32 v[186:187], v[106:107], v[186:187]
	v_pk_mul_f32 v[188:189], v[108:109], v[188:189]
	v_cvt_pk_f16_f32 v110, v182, v183
	v_cvt_pk_f16_f32 v111, v184, v185
	v_cvt_pk_f16_f32 v112, v186, v187
	v_cvt_pk_f16_f32 v113, v188, v189
	global_store_dwordx4 v[236:237], v[110:113], off sc1
	v_cvt_f32_f16_e32 v182, v150
	v_cvt_f32_f16_sdwa v183, v150 dst_sel:DWORD dst_unused:UNUSED_PAD src0_sel:WORD_1
	v_cvt_f32_f16_e32 v184, v151
	v_cvt_f32_f16_sdwa v185, v151 dst_sel:DWORD dst_unused:UNUSED_PAD src0_sel:WORD_1
	v_cvt_f32_f16_e32 v186, v152
	v_cvt_f32_f16_sdwa v187, v152 dst_sel:DWORD dst_unused:UNUSED_PAD src0_sel:WORD_1
	v_cvt_f32_f16_e32 v188, v153
	v_cvt_f32_f16_sdwa v189, v153 dst_sel:DWORD dst_unused:UNUSED_PAD src0_sel:WORD_1
	v_pk_mul_f32 v[182:183], v[102:103], v[182:183]
	v_pk_mul_f32 v[184:185], v[104:105], v[184:185]
	v_pk_mul_f32 v[186:187], v[98:99], v[186:187]
	v_pk_mul_f32 v[188:189], v[100:101], v[188:189]
	v_cvt_pk_f16_f32 v102, v182, v183
	v_cvt_pk_f16_f32 v103, v184, v185
	v_cvt_pk_f16_f32 v104, v186, v187
	v_cvt_pk_f16_f32 v105, v188, v189
	global_store_dwordx4 v[236:237], v[102:105], off offset:256 sc1
	v_add_u32_e32 v238, 128, v176
	v_mad_i64_i32 v[234:235], s[0:1], v238, s91, v[174:175]
	global_load_dwordx4 v[146:149], v[234:235], off
	global_load_dwordx4 v[150:153], v[234:235], off offset:256
	s_nop 1
	v_add_u32_e32 v238, 144, v176
	v_mad_i64_i32 v[234:235], s[0:1], v238, s91, v[174:175]
	global_load_dwordx4 v[110:113], v[234:235], off
	global_load_dwordx4 v[106:109], v[234:235], off offset:256
	s_waitcnt vmcnt(8)
; __device__ __forceinline__ unsigned cvt_pk_f16(float lo, float hi) { f32x2 v = {lo, hi}; h16x2 b = __builtin_convertvector(v, h16x2); return __builtin_bit_cast(unsigned, b); }
;     __device__ __forceinline__ void operator()(const f32x4 (&acc)[2][2][4][2], const Unit& u, int wr, int wc, int fr, int fq) const {
;     ...
;                         for (int bj = 0; bj < 2; ++bj) { const size_t row = (size_t)(row0 + ai * HALF + (2 * mp + mm) * 16);
;                             gv[mm][bj] = *(const h16x8*)(Gn + row * ldg + bj * HALF);
;                             if (n > 0) pv[mm][bj] = *(const h16x8*)(Mg + row * 1024 + col0 + bj * HALF); }
; #pragma unroll
;                     for (int mm = 0; mm < 2; ++mm)
; #pragma unroll
;                         for (int bj = 0; bj < 2; ++bj) { const int m = 2 * mp + mm; const size_t row = (size_t)(row0 + ai * HALF + m * 16);
;                             float o[8];
; #pragma unroll
;                             for (int e = 0; e < 8; ++e) { const float a = e < 4 ? acc[ai][bj][m][0][e] : acc[ai][bj][m][1][e - 4]; o[e] = a * (float)gv[mm][bj][e]; }
;                             if (n > 0) {
; #pragma unroll
;                                 for (int e = 0; e < 8; ++e) o[e] += (float)pv[mm][bj][e]; }
;                             u32x4 w; w.x = cvt_pk_f16(o[0], o[1]); w.y = cvt_pk_f16(o[2], o[3]); w.z = cvt_pk_f16(o[4], o[5]); w.w = cvt_pk_f16(o[6], o[7]);
;                             *(u32x4*)(Mg + row * 1024 + col0 + bj * HALF) = w; }
	v_add_u32_e32 v238, 32, v176
	v_lshlrev_b32_e32 v240, 11, v238
	v_lshl_add_u64 v[236:237], v[180:181], 0, v[240:241]
	v_cvt_f32_f16_e32 v182, v130
	v_cvt_f32_f16_sdwa v183, v130 dst_sel:DWORD dst_unused:UNUSED_PAD src0_sel:WORD_1
	v_cvt_f32_f16_e32 v184, v131
	v_cvt_f32_f16_sdwa v185, v131 dst_sel:DWORD dst_unused:UNUSED_PAD src0_sel:WORD_1
	v_cvt_f32_f16_e32 v186, v132
	v_cvt_f32_f16_sdwa v187, v132 dst_sel:DWORD dst_unused:UNUSED_PAD src0_sel:WORD_1
	v_cvt_f32_f16_e32 v188, v133
	v_cvt_f32_f16_sdwa v189, v133 dst_sel:DWORD dst_unused:UNUSED_PAD src0_sel:WORD_1
	v_pk_mul_f32 v[182:183], v[92:93], v[182:183]
	v_pk_mul_f32 v[184:185], v[94:95], v[184:185]
	v_pk_mul_f32 v[186:187], v[88:89], v[186:187]
	v_pk_mul_f32 v[188:189], v[90:91], v[188:189]
	v_cvt_pk_f16_f32 v92, v182, v183
	v_cvt_pk_f16_f32 v93, v184, v185
	v_cvt_pk_f16_f32 v94, v186, v187
	v_cvt_pk_f16_f32 v95, v188, v189
	global_store_dwordx4 v[236:237], v[92:95], off sc1
	v_cvt_f32_f16_e32 v182, v134
	v_cvt_f32_f16_sdwa v183, v134 dst_sel:DWORD dst_unused:UNUSED_PAD src0_sel:WORD_1
	v_cvt_f32_f16_e32 v184, v135
	v_cvt_f32_f16_sdwa v185, v135 dst_sel:DWORD dst_unused:UNUSED_PAD src0_sel:WORD_1
	v_cvt_f32_f16_e32 v186, v136
	v_cvt_f32_f16_sdwa v187, v136 dst_sel:DWORD dst_unused:UNUSED_PAD src0_sel:WORD_1
	v_cvt_f32_f16_e32 v188, v137
	v_cvt_f32_f16_sdwa v189, v137 dst_sel:DWORD dst_unused:UNUSED_PAD src0_sel:WORD_1
	v_pk_mul_f32 v[182:183], v[84:85], v[182:183]
	v_pk_mul_f32 v[184:185], v[86:87], v[184:185]
	v_pk_mul_f32 v[186:187], v[80:81], v[186:187]
	v_pk_mul_f32 v[188:189], v[82:83], v[188:189]
	v_cvt_pk_f16_f32 v84, v182, v183
	v_cvt_pk_f16_f32 v85, v184, v185
	v_cvt_pk_f16_f32 v86, v186, v187
	v_cvt_pk_f16_f32 v87, v188, v189
	global_store_dwordx4 v[236:237], v[84:87], off offset:256 sc1
	v_add_u32_e32 v238, 160, v176
	v_mad_i64_i32 v[234:235], s[0:1], v238, s91, v[174:175]
	global_load_dwordx4 v[130:133], v[234:235], off
	global_load_dwordx4 v[134:137], v[234:235], off offset:256
	s_nop 1
	v_add_u32_e32 v238, 176, v176
	v_mad_i64_i32 v[234:235], s[0:1], v238, s91, v[174:175]
	global_load_dwordx4 v[92:95], v[234:235], off
	global_load_dwordx4 v[88:91], v[234:235], off offset:256
	s_waitcnt vmcnt(12)
	v_add_u32_e32 v238, 48, v176
	v_lshlrev_b32_e32 v240, 11, v238
	v_lshl_add_u64 v[236:237], v[180:181], 0, v[240:241]
	v_cvt_f32_f16_e32 v182, v126
	v_cvt_f32_f16_sdwa v183, v126 dst_sel:DWORD dst_unused:UNUSED_PAD src0_sel:WORD_1
	v_cvt_f32_f16_e32 v184, v127
	v_cvt_f32_f16_sdwa v185, v127 dst_sel:DWORD dst_unused:UNUSED_PAD src0_sel:WORD_1
	v_cvt_f32_f16_e32 v186, v128
	v_cvt_f32_f16_sdwa v187, v128 dst_sel:DWORD dst_unused:UNUSED_PAD src0_sel:WORD_1
	v_cvt_f32_f16_e32 v188, v129
	v_cvt_f32_f16_sdwa v189, v129 dst_sel:DWORD dst_unused:UNUSED_PAD src0_sel:WORD_1
	v_pk_mul_f32 v[182:183], v[76:77], v[182:183]
	v_pk_mul_f32 v[184:185], v[78:79], v[184:185]
	v_pk_mul_f32 v[186:187], v[72:73], v[186:187]
	v_pk_mul_f32 v[188:189], v[74:75], v[188:189]
	v_cvt_pk_f16_f32 v76, v182, v183
	v_cvt_pk_f16_f32 v77, v184, v185
	v_cvt_pk_f16_f32 v78, v186, v187
	v_cvt_pk_f16_f32 v79, v188, v189
	global_store_dwordx4 v[236:237], v[76:79], off sc1
	v_cvt_f32_f16_e32 v182, v122
	v_cvt_f32_f16_sdwa v183, v122 dst_sel:DWORD dst_unused:UNUSED_PAD src0_sel:WORD_1
	v_cvt_f32_f16_e32 v184, v123
	v_cvt_f32_f16_sdwa v185, v123 dst_sel:DWORD dst_unused:UNUSED_PAD src0_sel:WORD_1
	v_cvt_f32_f16_e32 v186, v124
	v_cvt_f32_f16_sdwa v187, v124 dst_sel:DWORD dst_unused:UNUSED_PAD src0_sel:WORD_1
	v_cvt_f32_f16_e32 v188, v125
	v_cvt_f32_f16_sdwa v189, v125 dst_sel:DWORD dst_unused:UNUSED_PAD src0_sel:WORD_1
	v_pk_mul_f32 v[182:183], v[68:69], v[182:183]
	v_pk_mul_f32 v[184:185], v[70:71], v[184:185]
	v_pk_mul_f32 v[186:187], v[64:65], v[186:187]
	v_pk_mul_f32 v[188:189], v[66:67], v[188:189]
	v_cvt_pk_f16_f32 v68, v182, v183
	v_cvt_pk_f16_f32 v69, v184, v185
	v_cvt_pk_f16_f32 v70, v186, v187
	v_cvt_pk_f16_f32 v71, v188, v189
	global_store_dwordx4 v[236:237], v[68:71], off offset:256 sc1
	s_waitcnt vmcnt(10)
	v_add_u32_e32 v238, 128, v176
	v_lshlrev_b32_e32 v240, 11, v238
	v_lshl_add_u64 v[236:237], v[180:181], 0, v[240:241]
	v_cvt_f32_f16_e32 v182, v146
	v_cvt_f32_f16_sdwa v183, v146 dst_sel:DWORD dst_unused:UNUSED_PAD src0_sel:WORD_1
	v_cvt_f32_f16_e32 v184, v147
	v_cvt_f32_f16_sdwa v185, v147 dst_sel:DWORD dst_unused:UNUSED_PAD src0_sel:WORD_1
	v_cvt_f32_f16_e32 v186, v148
	v_cvt_f32_f16_sdwa v187, v148 dst_sel:DWORD dst_unused:UNUSED_PAD src0_sel:WORD_1
	v_cvt_f32_f16_e32 v188, v149
	v_cvt_f32_f16_sdwa v189, v149 dst_sel:DWORD dst_unused:UNUSED_PAD src0_sel:WORD_1
	v_pk_mul_f32 v[182:183], v[60:61], v[182:183]
	v_pk_mul_f32 v[184:185], v[62:63], v[184:185]
	v_pk_mul_f32 v[186:187], v[56:57], v[186:187]
	v_pk_mul_f32 v[188:189], v[58:59], v[188:189]
	v_cvt_pk_f16_f32 v60, v182, v183
	v_cvt_pk_f16_f32 v61, v184, v185
	v_cvt_pk_f16_f32 v62, v186, v187
	v_cvt_pk_f16_f32 v63, v188, v189
	global_store_dwordx4 v[236:237], v[60:63], off sc1
	v_cvt_f32_f16_e32 v182, v150
	v_cvt_f32_f16_sdwa v183, v150 dst_sel:DWORD dst_unused:UNUSED_PAD src0_sel:WORD_1
	v_cvt_f32_f16_e32 v184, v151
	v_cvt_f32_f16_sdwa v185, v151 dst_sel:DWORD dst_unused:UNUSED_PAD src0_sel:WORD_1
	v_cvt_f32_f16_e32 v186, v152
	v_cvt_f32_f16_sdwa v187, v152 dst_sel:DWORD dst_unused:UNUSED_PAD src0_sel:WORD_1
	v_cvt_f32_f16_e32 v188, v153
	v_cvt_f32_f16_sdwa v189, v153 dst_sel:DWORD dst_unused:UNUSED_PAD src0_sel:WORD_1
	v_pk_mul_f32 v[182:183], v[52:53], v[182:183]
	v_pk_mul_f32 v[184:185], v[54:55], v[184:185]
	v_pk_mul_f32 v[186:187], v[48:49], v[186:187]
	v_pk_mul_f32 v[188:189], v[50:51], v[188:189]
	v_cvt_pk_f16_f32 v52, v182, v183
	v_cvt_pk_f16_f32 v53, v184, v185
	v_cvt_pk_f16_f32 v54, v186, v187
	v_cvt_pk_f16_f32 v55, v188, v189
	global_store_dwordx4 v[236:237], v[52:55], off offset:256 sc1
	s_waitcnt vmcnt(10)
; __device__ __forceinline__ unsigned cvt_pk_f16(float lo, float hi) { f32x2 v = {lo, hi}; h16x2 b = __builtin_convertvector(v, h16x2); return __builtin_bit_cast(unsigned, b); }
;     __device__ __forceinline__ void operator()(const f32x4 (&acc)[2][2][4][2], const Unit& u, int wr, int wc, int fr, int fq) const {
;     ...
;                         for (int bj = 0; bj < 2; ++bj) { const size_t row = (size_t)(row0 + ai * HALF + (2 * mp + mm) * 16);
;                             gv[mm][bj] = *(const h16x8*)(Gn + row * ldg + bj * HALF);
;                             if (n > 0) pv[mm][bj] = *(const h16x8*)(Mg + row * 1024 + col0 + bj * HALF); }
; #pragma unroll
;                     for (int mm = 0; mm < 2; ++mm)
; #pragma unroll
;                         for (int bj = 0; bj < 2; ++bj) { const int m = 2 * mp + mm; const size_t row = (size_t)(row0 + ai * HALF + m * 16);
;                             float o[8];
; #pragma unroll
;                             for (int e = 0; e < 8; ++e) { const float a = e < 4 ? acc[ai][bj][m][0][e] : acc[ai][bj][m][1][e - 4]; o[e] = a * (float)gv[mm][bj][e]; }
;                             if (n > 0) {
; #pragma unroll
;                                 for (int e = 0; e < 8; ++e) o[e] += (float)pv[mm][bj][e]; }
;                             u32x4 w; w.x = cvt_pk_f16(o[0], o[1]); w.y = cvt_pk_f16(o[2], o[3]); w.z = cvt_pk_f16(o[4], o[5]); w.w = cvt_pk_f16(o[6], o[7]);
;                             *(u32x4*)(Mg + row * 1024 + col0 + bj * HALF) = w; }
	v_add_u32_e32 v238, 144, v176
	v_lshlrev_b32_e32 v240, 11, v238
	v_lshl_add_u64 v[236:237], v[180:181], 0, v[240:241]
	v_cvt_f32_f16_e32 v182, v110
	v_cvt_f32_f16_sdwa v183, v110 dst_sel:DWORD dst_unused:UNUSED_PAD src0_sel:WORD_1
	v_cvt_f32_f16_e32 v184, v111
	v_cvt_f32_f16_sdwa v185, v111 dst_sel:DWORD dst_unused:UNUSED_PAD src0_sel:WORD_1
	v_cvt_f32_f16_e32 v186, v112
	v_cvt_f32_f16_sdwa v187, v112 dst_sel:DWORD dst_unused:UNUSED_PAD src0_sel:WORD_1
	v_cvt_f32_f16_e32 v188, v113
	v_cvt_f32_f16_sdwa v189, v113 dst_sel:DWORD dst_unused:UNUSED_PAD src0_sel:WORD_1
	v_pk_mul_f32 v[182:183], v[44:45], v[182:183]
	v_pk_mul_f32 v[184:185], v[46:47], v[184:185]
	v_pk_mul_f32 v[186:187], v[40:41], v[186:187]
	v_pk_mul_f32 v[188:189], v[42:43], v[188:189]
	v_cvt_pk_f16_f32 v44, v182, v183
	v_cvt_pk_f16_f32 v45, v184, v185
	v_cvt_pk_f16_f32 v46, v186, v187
	v_cvt_pk_f16_f32 v47, v188, v189
	global_store_dwordx4 v[236:237], v[44:47], off sc1
	v_cvt_f32_f16_e32 v182, v106
	v_cvt_f32_f16_sdwa v183, v106 dst_sel:DWORD dst_unused:UNUSED_PAD src0_sel:WORD_1
	v_cvt_f32_f16_e32 v184, v107
	v_cvt_f32_f16_sdwa v185, v107 dst_sel:DWORD dst_unused:UNUSED_PAD src0_sel:WORD_1
	v_cvt_f32_f16_e32 v186, v108
	v_cvt_f32_f16_sdwa v187, v108 dst_sel:DWORD dst_unused:UNUSED_PAD src0_sel:WORD_1
	v_cvt_f32_f16_e32 v188, v109
	v_cvt_f32_f16_sdwa v189, v109 dst_sel:DWORD dst_unused:UNUSED_PAD src0_sel:WORD_1
	v_pk_mul_f32 v[182:183], v[28:29], v[182:183]
	v_pk_mul_f32 v[184:185], v[30:31], v[184:185]
	v_pk_mul_f32 v[186:187], v[24:25], v[186:187]
	v_pk_mul_f32 v[188:189], v[26:27], v[188:189]
	v_cvt_pk_f16_f32 v28, v182, v183
	v_cvt_pk_f16_f32 v29, v184, v185
	v_cvt_pk_f16_f32 v30, v186, v187
	v_cvt_pk_f16_f32 v31, v188, v189
	global_store_dwordx4 v[236:237], v[28:31], off offset:256 sc1
	s_waitcnt vmcnt(8)
	v_add_u32_e32 v238, 160, v176
	v_lshlrev_b32_e32 v240, 11, v238
	v_lshl_add_u64 v[236:237], v[180:181], 0, v[240:241]
	v_cvt_f32_f16_e32 v182, v130
	v_cvt_f32_f16_sdwa v183, v130 dst_sel:DWORD dst_unused:UNUSED_PAD src0_sel:WORD_1
	v_cvt_f32_f16_e32 v184, v131
	v_cvt_f32_f16_sdwa v185, v131 dst_sel:DWORD dst_unused:UNUSED_PAD src0_sel:WORD_1
	v_cvt_f32_f16_e32 v186, v132
	v_cvt_f32_f16_sdwa v187, v132 dst_sel:DWORD dst_unused:UNUSED_PAD src0_sel:WORD_1
	v_cvt_f32_f16_e32 v188, v133
	v_cvt_f32_f16_sdwa v189, v133 dst_sel:DWORD dst_unused:UNUSED_PAD src0_sel:WORD_1
	v_pk_mul_f32 v[182:183], v[20:21], v[182:183]
	v_pk_mul_f32 v[184:185], v[22:23], v[184:185]
	v_pk_mul_f32 v[186:187], v[16:17], v[186:187]
	v_pk_mul_f32 v[188:189], v[18:19], v[188:189]
	v_cvt_pk_f16_f32 v20, v182, v183
	v_cvt_pk_f16_f32 v21, v184, v185
	v_cvt_pk_f16_f32 v22, v186, v187
	v_cvt_pk_f16_f32 v23, v188, v189
	global_store_dwordx4 v[236:237], v[20:23], off sc1
	v_cvt_f32_f16_e32 v182, v134
	v_cvt_f32_f16_sdwa v183, v134 dst_sel:DWORD dst_unused:UNUSED_PAD src0_sel:WORD_1
	v_cvt_f32_f16_e32 v184, v135
	v_cvt_f32_f16_sdwa v185, v135 dst_sel:DWORD dst_unused:UNUSED_PAD src0_sel:WORD_1
	v_cvt_f32_f16_e32 v186, v136
	v_cvt_f32_f16_sdwa v187, v136 dst_sel:DWORD dst_unused:UNUSED_PAD src0_sel:WORD_1
	v_cvt_f32_f16_e32 v188, v137
	v_cvt_f32_f16_sdwa v189, v137 dst_sel:DWORD dst_unused:UNUSED_PAD src0_sel:WORD_1
	v_pk_mul_f32 v[182:183], v[32:33], v[182:183]
	v_pk_mul_f32 v[184:185], v[34:35], v[184:185]
	v_pk_mul_f32 v[186:187], v[36:37], v[186:187]
	v_pk_mul_f32 v[188:189], v[38:39], v[188:189]
	v_cvt_pk_f16_f32 v32, v182, v183
	v_cvt_pk_f16_f32 v33, v184, v185
	v_cvt_pk_f16_f32 v34, v186, v187
	v_cvt_pk_f16_f32 v35, v188, v189
	global_store_dwordx4 v[236:237], v[32:35], off offset:256 sc1
	s_waitcnt vmcnt(8)
	v_add_u32_e32 v238, 176, v176
	v_lshlrev_b32_e32 v240, 11, v238
	v_lshl_add_u64 v[236:237], v[180:181], 0, v[240:241]
	v_cvt_f32_f16_e32 v182, v92
	v_cvt_f32_f16_sdwa v183, v92 dst_sel:DWORD dst_unused:UNUSED_PAD src0_sel:WORD_1
	v_cvt_f32_f16_e32 v184, v93
	v_cvt_f32_f16_sdwa v185, v93 dst_sel:DWORD dst_unused:UNUSED_PAD src0_sel:WORD_1
	v_cvt_f32_f16_e32 v186, v94
	v_cvt_f32_f16_sdwa v187, v94 dst_sel:DWORD dst_unused:UNUSED_PAD src0_sel:WORD_1
	v_cvt_f32_f16_e32 v188, v95
	v_cvt_f32_f16_sdwa v189, v95 dst_sel:DWORD dst_unused:UNUSED_PAD src0_sel:WORD_1
	v_pk_mul_f32 v[182:183], v[4:5], v[182:183]
	v_pk_mul_f32 v[184:185], v[6:7], v[184:185]
	v_pk_mul_f32 v[186:187], v[0:1], v[186:187]
	v_pk_mul_f32 v[188:189], v[2:3], v[188:189]
	v_cvt_pk_f16_f32 v4, v182, v183
	v_cvt_pk_f16_f32 v5, v184, v185
	v_cvt_pk_f16_f32 v6, v186, v187
	v_cvt_pk_f16_f32 v7, v188, v189
	global_store_dwordx4 v[236:237], v[4:7], off sc1
	v_cvt_f32_f16_e32 v182, v88
	v_cvt_f32_f16_sdwa v183, v88 dst_sel:DWORD dst_unused:UNUSED_PAD src0_sel:WORD_1
	v_cvt_f32_f16_e32 v184, v89
	v_cvt_f32_f16_sdwa v185, v89 dst_sel:DWORD dst_unused:UNUSED_PAD src0_sel:WORD_1
	v_cvt_f32_f16_e32 v186, v90
	v_cvt_f32_f16_sdwa v187, v90 dst_sel:DWORD dst_unused:UNUSED_PAD src0_sel:WORD_1
	v_cvt_f32_f16_e32 v188, v91
	v_cvt_f32_f16_sdwa v189, v91 dst_sel:DWORD dst_unused:UNUSED_PAD src0_sel:WORD_1
	v_pk_mul_f32 v[182:183], v[8:9], v[182:183]
	v_pk_mul_f32 v[184:185], v[10:11], v[184:185]
	v_pk_mul_f32 v[186:187], v[12:13], v[186:187]
	v_pk_mul_f32 v[188:189], v[14:15], v[188:189]
	v_cvt_pk_f16_f32 v8, v182, v183
	v_cvt_pk_f16_f32 v9, v184, v185
	v_cvt_pk_f16_f32 v10, v186, v187
	v_cvt_pk_f16_f32 v11, v188, v189
	global_store_dwordx4 v[236:237], v[8:11], off offset:256 sc1
	s_branch .Lbrepi_done
